# v8 with static s_setprio 1 for waves 4-7 (no per-segment toggles)
# baseline (speedup 1.0000x reference)
.LBB0_5:
	s_or_b64 exec, exec, s[0:1]
	s_cmp_lt_u32 s4, 0x100
	s_cbranch_scc1 .Lprio_lo
	s_setprio 1
.Lprio_lo:
	s_lshr_b32 s1, s4, 6
	s_lshl_b32 s0, s90, 3
	v_writelane_b32 v252, s1, 13
	s_add_i32 s0, s1, s0
	v_writelane_b32 v252, s0, 14
	s_lshl_b32 s0, s80, 9
	v_writelane_b32 v252, s0, 15
	s_lshl_b32 s85, s80, 3
	s_lshl_b32 s6, s90, 9
	v_writelane_b32 v252, s1, 16
	v_and_b32_e32 v198, 63, v0
	v_readlane_b32 s0, v252, 0
	v_readlane_b32 s1, v252, 1
	s_mov_b64 s[4:5], s[0:1]
	s_cmp_lt_i32 s4, 1
	v_readlane_b32 s2, v252, 2
	v_readlane_b32 s3, v252, 3
	s_cselect_b64 s[0:1], -1, 0
	s_cmp_gt_i32 s5, 0
	s_cselect_b64 s[2:3], -1, 0
	s_and_b64 s[38:39], s[0:1], s[2:3]
	s_andn2_b64 vcc, exec, s[38:39]
	v_or_b32_e32 v194, s6, v0
	s_cbranch_vccnz .LBB0_152
	v_writelane_b32 v252, s6, 17
	v_writelane_b32 v252, s38, 19
	s_cmpk_gt_i32 s80, 0x80
	s_mov_b32 s15, s85
	v_writelane_b32 v252, s39, 20
	s_mov_b32 s14, s80
	v_readlane_b32 s4, v252, 4
	v_readlane_b32 s5, v252, 5
	s_load_dwordx8 s[16:23], s[4:5], 0x0
	s_load_dwordx2 s[0:1], s[4:5], 0x20
	s_waitcnt lgkmcnt(0)
	v_writelane_b32 v252, s16, 21
	s_nop 1
	v_writelane_b32 v252, s17, 22
	v_writelane_b32 v252, s18, 23
	v_writelane_b32 v252, s19, 24
	v_writelane_b32 v252, s20, 25
	v_writelane_b32 v252, s21, 26
	v_writelane_b32 v252, s22, 27
	v_writelane_b32 v252, s23, 28
	v_writelane_b32 v252, s0, 29
	s_nop 1
	v_writelane_b32 v252, s1, 30
	s_load_dwordx4 s[0:3], s[4:5], 0x90
	s_waitcnt lgkmcnt(0)
	v_writelane_b32 v252, s0, 31
	s_nop 1
	v_writelane_b32 v252, s1, 32
	v_writelane_b32 v252, s2, 33
	v_writelane_b32 v252, s3, 34
	s_load_dwordx2 s[0:1], s[4:5], 0xd8
	s_waitcnt lgkmcnt(0)
	v_writelane_b32 v252, s0, 35
	s_nop 1
	v_writelane_b32 v252, s1, 36
	s_cselect_b64 s[0:1], -1, 0
	s_cmpk_lt_i32 s80, 0x81
	s_cselect_b64 s[2:3], -1, 0
	v_writelane_b32 v252, s2, 37
	s_nop 1
	v_writelane_b32 v252, s3, 38
	s_and_b64 s[2:3], s[2:3], exec
	s_cselect_b32 s2, 0, 64
	s_cmp_ge_i32 s90, s2
	v_writelane_b32 v252, s2, 39
	s_cselect_b64 s[2:3], -1, 0
	v_writelane_b32 v252, s2, 41
	s_and_b64 s[0:1], s[0:1], s[2:3]
	s_cmp_gt_i32 s90, 63
	v_writelane_b32 v252, s3, 42
	s_mov_b32 s2, s90
	v_writelane_b32 v252, s2, 43
	s_nop 1
	v_writelane_b32 v252, s3, 44
	s_cselect_b64 s[2:3], -1, 0
	s_or_b64 s[0:1], s[0:1], s[2:3]
	s_and_b64 vcc, exec, s[0:1]
	s_cbranch_vccnz .LBB0_41
	v_cmp_eq_u32_e64 s[0:1], 1, v0
	s_load_dwordx2 s[2:3], s[4:5], 0xf0
	s_load_dwordx16 s[52:67], s[4:5], 0x28
	v_writelane_b32 v252, s0, 45
	v_mov_b32_e32 v7, 0
	v_and_b32_e32 v1, 15, v0
	v_writelane_b32 v252, s1, 46
	v_cmp_eq_u32_e64 s[0:1], 2, v0
	v_lshrrev_b32_e32 v4, 4, v0
	v_lshlrev_b32_e32 v2, 10, v4
	v_writelane_b32 v252, s0, 47
	v_lshlrev_b32_e32 v5, 2, v1
	v_lshlrev_b32_e32 v10, 3, v0
	v_writelane_b32 v252, s1, 48
	v_cmp_eq_u32_e64 s[0:1], 3, v0
	v_mov_b32_e32 v11, v7
	v_add3_u32 v36, 0, v2, v5
	v_writelane_b32 v252, s0, 49
	s_waitcnt lgkmcnt(0)
	v_lshl_add_u64 v[2:3], s[2:3], 0, v[10:11]
	s_mov_b64 s[4:5], 0x37800000
	v_writelane_b32 v252, s1, 50
	v_cmp_eq_u32_e64 s[0:1], 4, v0
	v_lshl_add_u64 v[12:13], v[2:3], 0, s[4:5]
	s_mov_b32 s42, s14
	v_writelane_b32 v252, s0, 51
	v_lshrrev_b32_e32 v39, 6, v0
	v_lshlrev_b32_e32 v2, 2, v39
	v_writelane_b32 v252, s1, 52
	s_add_u32 s0, s2, 0x34000000
	v_readlane_b32 s44, v252, 43
	v_readlane_b32 s45, v252, 44
	s_addc_u32 s1, s3, 0
	s_ashr_i32 s45, s44, 31
	s_lshl_b64 s[6:7], s[44:45], 12
	s_add_u32 s4, s64, s6
	s_addc_u32 s5, s65, s7
	s_ashr_i32 s43, s14, 31
	s_lshl_b64 s[64:65], s[42:43], 12
	s_add_u32 s94, s62, s6
	s_addc_u32 s95, s63, s7
	v_lshl_or_b32 v2, v198, 6, v2
	s_add_u32 s80, s60, s6
	v_add_u32_e32 v2, 0, v2
	s_addc_u32 s81, s61, s7
	v_add_u32_e32 v41, 0x11200, v2
	s_add_u32 s50, s58, s6
	v_add_u32_e32 v2, 0, v5
	s_addc_u32 s51, s59, s7
	v_lshlrev_b32_e32 v6, 2, v4
	v_add_u32_e32 v42, 0x4200, v2
	s_mul_hi_i32 s6, s44, 0xa0000
	s_mul_i32 s7, s44, 0xa0000
	v_mul_hi_u32_u24_e32 v2, 0x500, v39
	v_mul_u32_u24_e32 v5, 0x500, v39
	v_lshl_add_u64 v[14:15], s[54:55], 0, v[6:7]
	v_lshl_add_u64 v[16:17], s[52:53], 0, v[6:7]
	v_or_b32_e32 v3, s6, v2
	v_or_b32_e32 v2, s7, v5
	v_lshlrev_b32_e32 v6, 4, v198
	v_lshl_add_u64 v[2:3], v[2:3], 0, v[6:7]
	v_lshl_add_u64 v[18:19], s[0:1], 0, v[2:3]
	v_mul_hi_u32_u24_e32 v2, 0x500, v4
	v_mul_u32_u24_e32 v5, 0x500, v4
	v_or_b32_e32 v3, s6, v2
	v_or_b32_e32 v2, s7, v5
	v_lshl_or_b32 v2, v1, 4, v2
	v_lshl_add_u64 v[2:3], s[0:1], 0, v[2:3]
	s_mov_b64 s[0:1], 0x400
	v_lshl_add_u64 v[20:21], v[2:3], 0, s[0:1]
	s_lshl_b64 s[0:1], s[44:45], 18
	v_lshlrev_b32_e32 v2, 10, v39
	v_or3_b32 v2, s0, v2, v6
	v_mov_b32_e32 v3, s1
	v_lshlrev_b32_e32 v8, 2, v0
	v_lshl_add_u64 v[2:3], s[2:3], 0, v[2:3]
	s_mov_b32 s2, s44
	v_add_u32_e32 v38, 0, v8
	s_mov_b64 s[0:1], 0x36800000
	v_writelane_b32 v252, s2, 43
	v_cmp_eq_u32_e64 s[16:17], 5, v0
	v_cmp_eq_u32_e64 s[18:19], 6, v0
	v_cmp_eq_u32_e64 s[20:21], 7, v0
	v_cmp_eq_u32_e64 s[22:23], 8, v0
	v_cmp_eq_u32_e64 s[24:25], 9, v0
	v_lshrrev_b32_e32 v37, 1, v198
	v_or_b32_e32 v11, 0xfffffe00, v0
	v_add_u32_e32 v40, 0x4200, v38
	v_mov_b32_e32 v9, v7
	s_lshl_b32 s70, s14, 6
	v_lshlrev_b32_e32 v43, 8, v4
	s_mul_hi_i32 s85, s14, 0xa0000
	s_mul_i32 s84, s14, 0xa0000
	v_lshlrev_b32_e32 v44, 4, v39
	v_lshrrev_b32_e32 v45, 2, v0
	v_lshlrev_b32_e32 v46, 6, v4
	v_lshlrev_b32_e32 v47, 5, v0
	v_lshl_add_u64 v[22:23], v[2:3], 0, s[0:1]
	s_mov_b32 s71, 0x3fb8aa3b
	s_mov_b32 s72, 0xc2ce8ed0
	s_mov_b32 s73, 0x42b17218
	v_mov_b32_e32 v48, 0x7f800000
	v_lshlrev_b32_e32 v49, 2, v198
	s_brev_b32 s74, 18
	s_mov_b32 s75, 0xfe5163ab
	s_mov_b32 s69, 0x3c439041
	s_mov_b32 s0, 0xdb629599
	s_mov_b32 s1, 0xf534ddc0
	s_mov_b32 s33, 0xfc2757d1
	s_mov_b32 s68, 0x4e441529
	s_mov_b32 s88, 0xa2f9836e
	s_mov_b32 s89, 0x3fc90fda
	s_mov_b32 s8, 0x3f22f983
	s_mov_b32 s9, 0xbfc90fda
	v_mov_b32_e32 v50, 0x3c0881c4
	v_mov_b32_e32 v51, 0xbab64f3b
	s_brev_b32 s10, 1
	s_movk_i32 s11, 0x1f8
	s_movk_i32 s12, 0x7fff
	s_mov_b32 s13, 0xffff0000
	v_not_b32_e32 v52, 63
	v_not_b32_e32 v53, 31
	v_mov_b32_e32 v54, 0x7fc00000
	v_cmp_eq_u32_e64 s[26:27], 10, v0
	v_cmp_eq_u32_e64 s[28:29], 11, v0
	v_cmp_eq_u32_e64 s[30:31], 12, v0
	v_cmp_eq_u32_e64 s[34:35], 13, v0
	v_cmp_eq_u32_e64 s[36:37], 14, v0
	v_cmp_eq_u32_e64 s[38:39], 15, v0
	v_cmp_gt_u32_e64 s[40:41], 8, v1
	s_lshl_b32 s90, s44, 6
	s_lshl_b64 s[92:93], s[42:43], 18
	s_mov_b64 s[96:97], 0x80
	v_writelane_b32 v252, s3, 44
	s_mov_b32 s2, s44
	s_branch .LBB0_9
